# v14: + P0 forget-gate column fill with all 32 loads in flight; memory-row gains loaded up front
# baseline (speedup 1.0000x reference)
; template <int STAGE>
; __device__ __forceinline__ void p0_prologue(const Frame& F, const KArgs& a, const int w0, const int nw) {
;     ...
;     for (int i = F.tid; i < DM * 8; i += NTHREADS) wf[i + (i >> 5) * 4] = a.in[3][(size_t)(i >> 3) * INC + C_F + (i & 7)];
.LBB0_129:
	v_lshrrev_b32_e32 v11, 3, v0
	v_and_b32_e32 v13, 7, v0
	v_mul_u32_u24_e32 v12, 0x9020, v11
	v_lshrrev_b32_e32 v14, 5, v0
	v_lshl_add_u32 v12, v13, 2, v12
	v_lshl_add_u32 v14, v14, 4, v5
	v_add_u32_e32 v12, 0x3000, v12
	v_add_u32_e32 v15, 0x9000, v14
	s_mov_b64 s[98:99], s[14:15]
	global_load_dword v100, v12, s[98:99]
	s_add_u32 s98, s98, 0x240800
	s_addc_u32 s99, s99, 0
	global_load_dword v101, v12, s[98:99]
	s_add_u32 s98, s98, 0x240800
	s_addc_u32 s99, s99, 0
	global_load_dword v102, v12, s[98:99]
	s_add_u32 s98, s98, 0x240800
	s_addc_u32 s99, s99, 0
	global_load_dword v103, v12, s[98:99]
	s_add_u32 s98, s98, 0x240800
	s_addc_u32 s99, s99, 0
	global_load_dword v104, v12, s[98:99]
	s_add_u32 s98, s98, 0x240800
	s_addc_u32 s99, s99, 0
	global_load_dword v105, v12, s[98:99]
	s_add_u32 s98, s98, 0x240800
	s_addc_u32 s99, s99, 0
	global_load_dword v106, v12, s[98:99]
	s_add_u32 s98, s98, 0x240800
	s_addc_u32 s99, s99, 0
	global_load_dword v107, v12, s[98:99]
	s_add_u32 s98, s98, 0x240800
	s_addc_u32 s99, s99, 0
	global_load_dword v108, v12, s[98:99]
	s_add_u32 s98, s98, 0x240800
	s_addc_u32 s99, s99, 0
	global_load_dword v109, v12, s[98:99]
	s_add_u32 s98, s98, 0x240800
	s_addc_u32 s99, s99, 0
	global_load_dword v110, v12, s[98:99]
	s_add_u32 s98, s98, 0x240800
	s_addc_u32 s99, s99, 0
	global_load_dword v111, v12, s[98:99]
	s_add_u32 s98, s98, 0x240800
	s_addc_u32 s99, s99, 0
	global_load_dword v112, v12, s[98:99]
	s_add_u32 s98, s98, 0x240800
	s_addc_u32 s99, s99, 0
	global_load_dword v113, v12, s[98:99]
	s_add_u32 s98, s98, 0x240800
	s_addc_u32 s99, s99, 0
	global_load_dword v114, v12, s[98:99]
	s_add_u32 s98, s98, 0x240800
	s_addc_u32 s99, s99, 0
	global_load_dword v115, v12, s[98:99]
	s_add_u32 s98, s98, 0x240800
	s_addc_u32 s99, s99, 0
	global_load_dword v116, v12, s[98:99]
	s_add_u32 s98, s98, 0x240800
	s_addc_u32 s99, s99, 0
	global_load_dword v117, v12, s[98:99]
	s_add_u32 s98, s98, 0x240800
	s_addc_u32 s99, s99, 0
	global_load_dword v118, v12, s[98:99]
	s_add_u32 s98, s98, 0x240800
	s_addc_u32 s99, s99, 0
	global_load_dword v119, v12, s[98:99]
	s_add_u32 s98, s98, 0x240800
	s_addc_u32 s99, s99, 0
	global_load_dword v120, v12, s[98:99]
	s_add_u32 s98, s98, 0x240800
	s_addc_u32 s99, s99, 0
	global_load_dword v121, v12, s[98:99]
	s_add_u32 s98, s98, 0x240800
	s_addc_u32 s99, s99, 0
	global_load_dword v122, v12, s[98:99]
	s_add_u32 s98, s98, 0x240800
	s_addc_u32 s99, s99, 0
	global_load_dword v123, v12, s[98:99]
	s_add_u32 s98, s98, 0x240800
	s_addc_u32 s99, s99, 0
	global_load_dword v124, v12, s[98:99]
	s_add_u32 s98, s98, 0x240800
	s_addc_u32 s99, s99, 0
	global_load_dword v125, v12, s[98:99]
	s_add_u32 s98, s98, 0x240800
	s_addc_u32 s99, s99, 0
	global_load_dword v126, v12, s[98:99]
	s_add_u32 s98, s98, 0x240800
	s_addc_u32 s99, s99, 0
	global_load_dword v127, v12, s[98:99]
	s_add_u32 s98, s98, 0x240800
	s_addc_u32 s99, s99, 0
	global_load_dword v128, v12, s[98:99]
	s_add_u32 s98, s98, 0x240800
	s_addc_u32 s99, s99, 0
	global_load_dword v129, v12, s[98:99]
	s_add_u32 s98, s98, 0x240800
	s_addc_u32 s99, s99, 0
	global_load_dword v130, v12, s[98:99]
	s_add_u32 s98, s98, 0x240800
	s_addc_u32 s99, s99, 0
	global_load_dword v131, v12, s[98:99]
	s_waitcnt vmcnt(0)
	ds_write_b32 v14, v100
	ds_write_b32 v14, v101 offset:2304
	ds_write_b32 v14, v102 offset:4608
	ds_write_b32 v14, v103 offset:6912
	ds_write_b32 v14, v104 offset:9216
	ds_write_b32 v14, v105 offset:11520
	ds_write_b32 v14, v106 offset:13824
	ds_write_b32 v14, v107 offset:16128
	ds_write_b32 v14, v108 offset:18432
	ds_write_b32 v14, v109 offset:20736
	ds_write_b32 v14, v110 offset:23040
	ds_write_b32 v14, v111 offset:25344
	ds_write_b32 v14, v112 offset:27648
	ds_write_b32 v14, v113 offset:29952
	ds_write_b32 v14, v114 offset:32256
	ds_write_b32 v14, v115 offset:34560
	ds_write_b32 v15, v116
	ds_write_b32 v15, v117 offset:2304
	ds_write_b32 v15, v118 offset:4608
	ds_write_b32 v15, v119 offset:6912
	ds_write_b32 v15, v120 offset:9216
	ds_write_b32 v15, v121 offset:11520
	ds_write_b32 v15, v122 offset:13824
	ds_write_b32 v15, v123 offset:16128
	ds_write_b32 v15, v124 offset:18432
	ds_write_b32 v15, v125 offset:20736
	ds_write_b32 v15, v126 offset:23040
	ds_write_b32 v15, v127 offset:25344
	ds_write_b32 v15, v128 offset:27648
	ds_write_b32 v15, v129 offset:29952
	ds_write_b32 v15, v130 offset:32256
	ds_write_b32 v15, v131 offset:34560
	s_or_b64 exec, exec, s[2:3]
	v_cmp_eq_u32_e64 s[2:3], 2, 0
	s_and_saveexec_b64 s[0:1], s[2:3]
	s_cbranch_execz .LBB0_132
	v_readlane_b32 s8, v252, 6
	v_readlane_b32 s14, v252, 12
	v_readlane_b32 s15, v252, 13
	v_lshrrev_b32_e32 v1, 3, v7
	v_lshrrev_b32_e32 v10, 3, v6
	s_mov_b32 s4, 0x9020
	v_mov_b64_e32 v[6:7], s[14:15]
	v_mad_u64_u32 v[8:9], s[2:3], v10, s4, v[6:7]
	v_mov_b32_e32 v3, 0
	v_mad_u64_u32 v[6:7], s[2:3], v1, s4, v[6:7]
	v_lshl_add_u64 v[8:9], v[8:9], 0, v[2:3]
	v_lshl_add_u64 v[2:3], v[6:7], 0, v[2:3]
	v_add_co_u32_e32 v6, vcc, 0x3000, v8
	v_and_b32_e32 v1, 0xffffffc, v1
	s_nop 0
	v_addc_co_u32_e32 v7, vcc, 0, v9, vcc
	v_add_co_u32_e32 v2, vcc, 0x3000, v2
	v_readlane_b32 s9, v252, 7
	s_nop 0
	v_addc_co_u32_e32 v3, vcc, 0, v3, vcc
	global_load_dword v6, v[6:7], off
	s_nop 0
	global_load_dword v2, v[2:3], off
	v_lshl_or_b32 v7, 32, 11, v5
	v_and_b32_e32 v3, 0xffffffc, v10
	v_add_u32_e32 v7, 0, v7
	v_lshl_add_u32 v3, v3, 2, v7
	v_readlane_b32 s10, v252, 8
	v_readlane_b32 s11, v252, 9
	v_readlane_b32 s12, v252, 10
	v_readlane_b32 s13, v252, 11
	v_readlane_b32 s16, v252, 14
	v_readlane_b32 s17, v252, 15
	v_readlane_b32 s18, v252, 16
	v_readlane_b32 s19, v252, 17
	v_readlane_b32 s20, v252, 18
	v_readlane_b32 s21, v252, 19
	v_readlane_b32 s22, v252, 20
	v_readlane_b32 s23, v252, 21
	v_lshl_add_u32 v1, v1, 2, v7
	s_waitcnt vmcnt(1)
	ds_write_b32 v3, v6
	s_waitcnt vmcnt(0)
	ds_write_b32 v1, v2 offset:2048

; __device__ __forceinline__ unsigned cvt_pk_bf16(float lo, float hi) { unsigned r; asm volatile("v_cvt_pk_bf16_f32 %0, %1, %2" : "=v"(r) : "v"(lo), "v"(hi)); return r; }
; template <int STAGE>
; __device__ __forceinline__ void p0_prologue(const Frame& F, const KArgs& a, const int w0, const int nw) {
;     ...
;     for (int r = F.gw; r < NMEM; r += F.NGW) {
;         const float* xr = a.in[1] + (size_t)r * DM; const float* g = a.in[13]; bf16* orow = (bf16*)(ws + WS_HM) + (size_t)r * DM;
;         f32x4 v[8]; float s = 0.f;
; #pragma unroll
;         for (int j = 0; j < 8; ++j) { v[j] = ((const f32x4*)xr)[lane + 64 * j]; s += (v[j][0] * v[j][0] + v[j][1] * v[j][1]) + (v[j][2] * v[j][2] + v[j][3] * v[j][3]); }
;         const float rstd = rsqrtf(wave_sum(s) * (1.f / DM) + RMS_EPS);
; #pragma unroll
;         for (int j = 0; j < 8; ++j) { const f32x4 gg = ((const f32x4*)g)[lane + 64 * j]; v[j] = v[j] * rstd * gg;
;             u32x2 w; w.x = cvt_pk_bf16(v[j][0], v[j][1]); w.y = cvt_pk_bf16(v[j][2], v[j][3]); *(u32x2*)(orow + 4 * (lane + 64 * j)) = w; }
;     }
.LBB0_142:
	global_load_dwordx4 v[100:103], v[6:7], off offset:1024
	global_load_dwordx4 v[104:107], v[6:7], off offset:2048
	global_load_dwordx4 v[108:111], v[6:7], off offset:3072
	global_load_dwordx4 v[112:115], v[8:9], off
	global_load_dwordx4 v[116:119], v[10:11], off
	global_load_dwordx4 v[120:123], v[12:13], off
	global_load_dwordx4 v[124:127], v[14:15], off
	global_load_dwordx4 v[26:29], v[18:19], off offset:-4096
	global_load_dwordx4 v[30:33], v[18:19], off offset:-3072
	global_load_dwordx4 v[34:37], v[18:19], off offset:-2048
	global_load_dwordx4 v[38:41], v[18:19], off
	global_load_dwordx4 v[42:45], v[18:19], off offset:-1024
	global_load_dwordx4 v[46:49], v[18:19], off offset:1024
	global_load_dwordx4 v[50:53], v[18:19], off offset:2048
	global_load_dwordx4 v[2:5], v[18:19], off offset:3072
	global_load_dwordx4 v[54:57], v[6:7], off
	s_add_i32 s5, s5, s94
	v_lshl_add_u64 v[18:19], v[18:19], 0, s[2:3]
	s_cmpk_lt_i32 s5, 0x400
	s_waitcnt vmcnt(8)
	v_mov_b32_e32 v60, v27
	s_waitcnt vmcnt(7)
	v_mov_b32_e32 v61, v31
	v_mov_b32_e32 v64, v29
	v_mov_b32_e32 v65, v33
	v_mov_b32_e32 v58, v26
	v_mov_b32_e32 v59, v30
	v_mov_b32_e32 v62, v28
	v_mov_b32_e32 v63, v32
	s_waitcnt vmcnt(6) lgkmcnt(7)
	v_pk_mul_f32 v[66:67], v[36:37], v[36:37]
	s_waitcnt lgkmcnt(6)
	v_pk_mul_f32 v[68:69], v[34:35], v[34:35]
	v_pk_mul_f32 v[60:61], v[60:61], v[60:61]
	v_pk_mul_f32 v[64:65], v[64:65], v[64:65]
	v_pk_mov_b32 v[82:83], v[68:69], v[66:67] op_sel:[1,0]
	v_mov_b32_e32 v69, v67
	v_pk_fma_f32 v[58:59], v[58:59], v[58:59], v[60:61]
	v_pk_fma_f32 v[60:61], v[62:63], v[62:63], v[64:65]
	s_waitcnt vmcnt(4)
	v_mul_f32_e32 v70, v43, v43
	v_mul_f32_e32 v72, v45, v45
	v_pk_add_f32 v[62:63], v[82:83], v[68:69]
	v_pk_add_f32 v[58:59], v[58:59], v[60:61]
	s_waitcnt lgkmcnt(0)
	v_mul_f32_e32 v81, v38, v38
	v_mul_f32_e32 v84, v39, v39
	v_mul_f32_e32 v85, v40, v40
	v_mul_f32_e32 v86, v41, v41
	v_pk_fma_f32 v[66:67], v[42:43], v[42:43], v[70:71] op_sel_hi:[1,1,0]
	v_pk_fma_f32 v[70:71], v[44:45], v[44:45], v[72:73] op_sel_hi:[1,1,0]
	v_pk_add_f32 v[60:61], v[62:63], v[62:63] op_sel:[0,1] op_sel_hi:[1,0]
	v_pk_add_f32 v[58:59], v[58:59], v[58:59] op_sel:[0,1] op_sel_hi:[1,0]
	s_waitcnt vmcnt(3)
	v_pk_mul_f32 v[74:75], v[48:49], v[48:49]
	v_pk_mul_f32 v[76:77], v[46:47], v[46:47]
	v_mov_b32_e32 v67, v85
	v_mov_b32_e32 v71, v86
	v_mov_b32_e32 v61, v84
	v_mov_b32_e32 v59, v81
	v_pk_mov_b32 v[72:73], v[76:77], v[74:75] op_sel:[1,0]
	v_mov_b32_e32 v77, v75
	v_pk_add_f32 v[62:63], v[66:67], v[70:71]
	v_pk_add_f32 v[58:59], v[58:59], v[60:61]
	s_waitcnt vmcnt(2)
	v_mul_f32_e32 v78, v51, v51
	v_mul_f32_e32 v80, v53, v53
	v_pk_add_f32 v[64:65], v[72:73], v[76:77]
	v_pk_add_f32 v[58:59], v[58:59], v[62:63]
	s_waitcnt vmcnt(1)
	v_mul_f32_e32 v87, v2, v2
	v_mul_f32_e32 v88, v3, v3
	v_mul_f32_e32 v89, v4, v4
	v_mul_f32_e32 v90, v5, v5
	v_pk_fma_f32 v[74:75], v[50:51], v[50:51], v[78:79] op_sel_hi:[1,1,0]
	v_pk_fma_f32 v[78:79], v[52:53], v[52:53], v[80:81] op_sel_hi:[1,1,0]
	v_pk_add_f32 v[64:65], v[64:65], v[64:65] op_sel:[0,1] op_sel_hi:[1,0]
	v_pk_add_f32 v[58:59], v[58:59], v[58:59] op_sel:[0,1] op_sel_hi:[1,0]
	v_mov_b32_e32 v75, v89
	v_mov_b32_e32 v79, v90
	v_mov_b32_e32 v65, v88
	v_mov_b32_e32 v59, v87
	v_pk_add_f32 v[66:67], v[74:75], v[78:79]
	v_pk_add_f32 v[58:59], v[58:59], v[64:65]
	s_nop 0
	v_pk_add_f32 v[58:59], v[58:59], v[66:67]
	s_nop 0
	v_add_f32_e32 v58, v58, v59
	ds_bpermute_b32 v59, v20, v58
	s_waitcnt lgkmcnt(0)
	v_add_f32_e32 v58, v58, v59
	ds_bpermute_b32 v59, v21, v58
	s_waitcnt lgkmcnt(0)
	v_add_f32_e32 v58, v58, v59
	ds_bpermute_b32 v59, v22, v58
	s_waitcnt lgkmcnt(0)
	v_add_f32_e32 v58, v58, v59
	ds_bpermute_b32 v59, v23, v58
	s_waitcnt lgkmcnt(0)
	v_add_f32_e32 v58, v58, v59
	ds_bpermute_b32 v59, v24, v58
	s_waitcnt lgkmcnt(0)
	v_add_f32_e32 v58, v58, v59
	ds_bpermute_b32 v59, v25, v58
	s_waitcnt lgkmcnt(0)
	v_add_f32_e32 v58, v58, v59
	v_fmamk_f32 v58, v58, 0x3a000000, v1
	v_mul_f32_e32 v59, 0x4b800000, v58
	v_cmp_gt_f32_e32 vcc, s4, v58
	s_nop 1
	v_cndmask_b32_e32 v58, v58, v59, vcc
	v_rsq_f32_e32 v58, v58
	s_nop 0
	v_mul_f32_e32 v59, 0x45800000, v58
	v_cndmask_b32_e32 v58, v58, v59, vcc
	v_pk_mul_f32 v[26:27], v[26:27], v[58:59] op_sel_hi:[1,0]
	v_pk_mul_f32 v[28:29], v[28:29], v[58:59] op_sel_hi:[1,0]
	s_waitcnt vmcnt(0)
	v_pk_mul_f32 v[26:27], v[54:55], v[26:27]
	v_pk_mul_f32 v[28:29], v[56:57], v[28:29]
	v_cvt_pk_bf16_f32 v26, v26, v27
	v_pk_mul_f32 v[30:31], v[30:31], v[58:59] op_sel_hi:[1,0]
	v_cvt_pk_bf16_f32 v27, v28, v29
	global_store_dwordx2 v[16:17], v[26:27], off
	v_pk_mul_f32 v[32:33], v[32:33], v[58:59] op_sel_hi:[1,0]
	v_pk_mul_f32 v[2:3], v[2:3], v[58:59] op_sel_hi:[1,0]
	v_pk_mul_f32 v[4:5], v[4:5], v[58:59] op_sel_hi:[1,0]
	v_pk_mul_f32 v[26:27], v[100:101], v[30:31]
	v_pk_mul_f32 v[28:29], v[102:103], v[32:33]
	v_cvt_pk_bf16_f32 v26, v26, v27
	v_pk_mul_f32 v[30:31], v[34:35], v[58:59] op_sel_hi:[1,0]
	v_cvt_pk_bf16_f32 v27, v28, v29
	global_store_dwordx2 v[16:17], v[26:27], off offset:512
	v_pk_mul_f32 v[32:33], v[36:37], v[58:59] op_sel_hi:[1,0]
	v_pk_mul_f32 v[26:27], v[104:105], v[30:31]
	v_pk_mul_f32 v[28:29], v[106:107], v[32:33]
	v_cvt_pk_bf16_f32 v26, v26, v27
	v_pk_mul_f32 v[30:31], v[42:43], v[58:59] op_sel_hi:[1,0]
	v_cvt_pk_bf16_f32 v27, v28, v29
	global_store_dwordx2 v[16:17], v[26:27], off offset:1024
	v_pk_mul_f32 v[32:33], v[44:45], v[58:59] op_sel_hi:[1,0]
	v_pk_mul_f32 v[26:27], v[108:109], v[30:31]
	v_pk_mul_f32 v[28:29], v[110:111], v[32:33]
	v_cvt_pk_bf16_f32 v26, v26, v27
	v_pk_mul_f32 v[30:31], v[38:39], v[58:59] op_sel_hi:[1,0]
	v_cvt_pk_bf16_f32 v27, v28, v29
	global_store_dwordx2 v[16:17], v[26:27], off offset:1536
	v_pk_mul_f32 v[32:33], v[40:41], v[58:59] op_sel_hi:[1,0]
	v_pk_mul_f32 v[26:27], v[30:31], v[112:113]
	v_pk_mul_f32 v[28:29], v[32:33], v[114:115]
	v_cvt_pk_bf16_f32 v26, v26, v27
	v_pk_mul_f32 v[30:31], v[46:47], v[58:59] op_sel_hi:[1,0]
	v_cvt_pk_bf16_f32 v27, v28, v29
	global_store_dwordx2 v[16:17], v[26:27], off offset:2048
	v_pk_mul_f32 v[32:33], v[48:49], v[58:59] op_sel_hi:[1,0]
	v_pk_mul_f32 v[26:27], v[30:31], v[116:117]
	v_pk_mul_f32 v[28:29], v[32:33], v[118:119]
	v_cvt_pk_bf16_f32 v26, v26, v27
	v_pk_mul_f32 v[30:31], v[50:51], v[58:59] op_sel_hi:[1,0]
	v_cvt_pk_bf16_f32 v27, v28, v29
	global_store_dwordx2 v[16:17], v[26:27], off offset:2560
	v_pk_mul_f32 v[32:33], v[52:53], v[58:59] op_sel_hi:[1,0]
	v_pk_mul_f32 v[26:27], v[30:31], v[120:121]
	v_pk_mul_f32 v[28:29], v[32:33], v[122:123]
	v_cvt_pk_bf16_f32 v26, v26, v27
	s_nop 0
	v_cvt_pk_bf16_f32 v27, v28, v29
	global_store_dwordx2 v[16:17], v[26:27], off offset:3072
	v_pk_mul_f32 v[2:3], v[2:3], v[124:125]
	v_pk_mul_f32 v[4:5], v[4:5], v[126:127]
	v_cvt_pk_bf16_f32 v2, v2, v3
	s_nop 0
	v_cvt_pk_bf16_f32 v3, v4, v5
	global_store_dwordx2 v[16:17], v[2:3], off offset:3584
	v_lshl_add_u64 v[16:17], v[16:17], 0, s[0:1]
	s_cbranch_scc1 .LBB0_142
